# grid barrier spin loops: poll back-off s_sleep 1 -> s_sleep 8 (less contention on the single release word)
# speedup vs baseline: 1.0050x; 1.0015x over previous
.LBB0_114:
	global_load_dword v17, v211, s[96:97] offset:1024 sc1
	global_load_dword v2, v211, s[96:97] offset:1280 sc1
	global_load_dword v3, v211, s[96:97] offset:1536 sc1
	global_load_dword v4, v211, s[96:97] offset:1792 sc1
	global_load_dword v5, v211, s[96:97] offset:2048 sc1
	global_load_dword v6, v211, s[96:97] offset:2304 sc1
	global_load_dword v7, v211, s[96:97] offset:2560 sc1
	global_load_dword v8, v211, s[96:97] offset:2816 sc1
	global_load_dword v9, v211, s[96:97] offset:3072 sc1
	global_load_dword v10, v211, s[96:97] offset:3328 sc1
	global_load_dword v11, v211, s[96:97] offset:3584 sc1
	global_load_dword v12, v211, s[96:97] offset:3840 sc1
	global_load_dword v13, v211, s[66:67] sc1
	global_load_dword v14, v211, s[28:29] sc1
	global_load_dword v15, v211, s[46:47] sc1
	global_load_dword v16, v211, s[64:65] sc1
	s_mov_b64 s[10:11], -1
	s_mov_b64 s[24:25], -1
	s_waitcnt vmcnt(14)
	v_add_u32_e32 v18, v2, v17
	s_waitcnt vmcnt(13)
	v_add_u32_e32 v18, v18, v3
	s_waitcnt vmcnt(12)
	v_add_u32_e32 v18, v18, v4
	s_waitcnt vmcnt(11)
	v_add_u32_e32 v18, v18, v5
	s_waitcnt vmcnt(10)
	v_add_u32_e32 v18, v18, v6
	s_waitcnt vmcnt(9)
	v_add_u32_e32 v18, v18, v7
	s_waitcnt vmcnt(8)
	v_add_u32_e32 v18, v18, v8
	s_waitcnt vmcnt(7)
	v_add_u32_e32 v18, v18, v9
	s_waitcnt vmcnt(6)
	v_add_u32_e32 v18, v18, v10
	s_waitcnt vmcnt(5)
	v_add_u32_e32 v18, v18, v11
	s_waitcnt vmcnt(4)
	v_add_u32_e32 v18, v18, v12
	s_waitcnt vmcnt(3)
	v_add_u32_e32 v18, v18, v13
	s_waitcnt vmcnt(2)
	v_add_u32_e32 v18, v18, v14
	s_waitcnt vmcnt(1)
	v_add_u32_e32 v18, v18, v15
	s_waitcnt vmcnt(0)
	v_add_u32_e32 v18, v18, v16
	v_cmp_eq_u32_e32 vcc, s2, v18
	s_cbranch_vccnz .LBB0_113
	s_and_b32 s4, s3, 0xff
	s_cmp_eq_u32 s4, 0
	s_mov_b64 s[34:35], -1
	s_sleep 8
	s_cbranch_scc0 .LBB0_118
	global_load_dword v18, v211, s[84:85] sc1
	s_waitcnt vmcnt(0)
	v_cmp_eq_u32_e32 vcc, 0, v18
	s_cbranch_vccnz .LBB0_120
	s_mov_b64 s[34:35], 0

.LBB0_130:
	s_and_b32 s3, s2, 0xff
	s_mov_b64 s[40:41], -1
	s_cmp_lg_u32 s3, 0
	s_mov_b64 s[50:51], -1
	s_sleep 8
	s_cbranch_scc1 .LBB0_133
	global_load_dword v2, v211, s[84:85] sc1
	s_waitcnt vmcnt(0)
	v_cmp_eq_u32_e32 vcc, 0, v2
	s_cbranch_vccnz .LBB0_135
	s_mov_b64 s[50:51], 0
	s_mov_b64 s[42:43], -1

.LBB0_234:
	global_load_dword v17, v211, s[96:97] offset:1024 sc1
	global_load_dword v2, v211, s[96:97] offset:1280 sc1
	global_load_dword v3, v211, s[96:97] offset:1536 sc1
	global_load_dword v4, v211, s[96:97] offset:1792 sc1
	global_load_dword v5, v211, s[96:97] offset:2048 sc1
	global_load_dword v6, v211, s[96:97] offset:2304 sc1
	global_load_dword v7, v211, s[96:97] offset:2560 sc1
	global_load_dword v8, v211, s[96:97] offset:2816 sc1
	global_load_dword v9, v211, s[96:97] offset:3072 sc1
	global_load_dword v10, v211, s[96:97] offset:3328 sc1
	global_load_dword v11, v211, s[96:97] offset:3584 sc1
	global_load_dword v12, v211, s[96:97] offset:3840 sc1
	global_load_dword v13, v211, s[66:67] sc1
	global_load_dword v14, v211, s[28:29] sc1
	global_load_dword v15, v211, s[46:47] sc1
	global_load_dword v16, v211, s[64:65] sc1
	s_mov_b64 s[10:11], -1
	s_mov_b64 s[34:35], -1
	s_waitcnt vmcnt(14)
	v_add_u32_e32 v18, v2, v17
	s_waitcnt vmcnt(13)
	v_add_u32_e32 v18, v18, v3
	s_waitcnt vmcnt(12)
	v_add_u32_e32 v18, v18, v4
	s_waitcnt vmcnt(11)
	v_add_u32_e32 v18, v18, v5
	s_waitcnt vmcnt(10)
	v_add_u32_e32 v18, v18, v6
	s_waitcnt vmcnt(9)
	v_add_u32_e32 v18, v18, v7
	s_waitcnt vmcnt(8)
	v_add_u32_e32 v18, v18, v8
	s_waitcnt vmcnt(7)
	v_add_u32_e32 v18, v18, v9
	s_waitcnt vmcnt(6)
	v_add_u32_e32 v18, v18, v10
	s_waitcnt vmcnt(5)
	v_add_u32_e32 v18, v18, v11
	s_waitcnt vmcnt(4)
	v_add_u32_e32 v18, v18, v12
	s_waitcnt vmcnt(3)
	v_add_u32_e32 v18, v18, v13
	s_waitcnt vmcnt(2)
	v_add_u32_e32 v18, v18, v14
	s_waitcnt vmcnt(1)
	v_add_u32_e32 v18, v18, v15
	s_waitcnt vmcnt(0)
	v_add_u32_e32 v18, v18, v16
	v_cmp_eq_u32_e32 vcc, s2, v18
	s_cbranch_vccnz .LBB0_233
	s_and_b32 s4, s3, 0xff
	s_cmp_eq_u32 s4, 0
	s_mov_b64 s[38:39], -1
	s_sleep 8
	s_cbranch_scc0 .LBB0_238
	global_load_dword v18, v211, s[84:85] sc1
	s_waitcnt vmcnt(0)
	v_cmp_eq_u32_e32 vcc, 0, v18
	s_cbranch_vccnz .LBB0_240
	s_mov_b64 s[38:39], 0

.LBB0_250:
	s_and_b32 s3, s2, 0xff
	s_mov_b64 s[42:43], -1
	s_cmp_lg_u32 s3, 0
	s_mov_b64 s[62:63], -1
	s_sleep 8
	s_cbranch_scc1 .LBB0_253
	global_load_dword v2, v211, s[84:85] sc1
	s_waitcnt vmcnt(0)
	v_cmp_eq_u32_e32 vcc, 0, v2
	s_cbranch_vccnz .LBB0_255
	s_mov_b64 s[62:63], 0
	s_mov_b64 s[50:51], -1

.LBB0_361:
	global_load_dword v17, v211, s[96:97] offset:1024 sc1
	global_load_dword v2, v211, s[96:97] offset:1280 sc1
	global_load_dword v3, v211, s[96:97] offset:1536 sc1
	global_load_dword v4, v211, s[96:97] offset:1792 sc1
	global_load_dword v5, v211, s[96:97] offset:2048 sc1
	global_load_dword v6, v211, s[96:97] offset:2304 sc1
	global_load_dword v7, v211, s[96:97] offset:2560 sc1
	global_load_dword v8, v211, s[96:97] offset:2816 sc1
	global_load_dword v9, v211, s[96:97] offset:3072 sc1
	global_load_dword v10, v211, s[96:97] offset:3328 sc1
	global_load_dword v11, v211, s[96:97] offset:3584 sc1
	global_load_dword v12, v211, s[96:97] offset:3840 sc1
	global_load_dword v13, v211, s[66:67] sc1
	global_load_dword v14, v211, s[28:29] sc1
	global_load_dword v15, v211, s[46:47] sc1
	global_load_dword v16, v211, s[64:65] sc1
	s_mov_b64 s[24:25], -1
	s_mov_b64 s[34:35], -1
	s_waitcnt vmcnt(14)
	v_add_u32_e32 v18, v2, v17
	s_waitcnt vmcnt(13)
	v_add_u32_e32 v18, v18, v3
	s_waitcnt vmcnt(12)
	v_add_u32_e32 v18, v18, v4
	s_waitcnt vmcnt(11)
	v_add_u32_e32 v18, v18, v5
	s_waitcnt vmcnt(10)
	v_add_u32_e32 v18, v18, v6
	s_waitcnt vmcnt(9)
	v_add_u32_e32 v18, v18, v7
	s_waitcnt vmcnt(8)
	v_add_u32_e32 v18, v18, v8
	s_waitcnt vmcnt(7)
	v_add_u32_e32 v18, v18, v9
	s_waitcnt vmcnt(6)
	v_add_u32_e32 v18, v18, v10
	s_waitcnt vmcnt(5)
	v_add_u32_e32 v18, v18, v11
	s_waitcnt vmcnt(4)
	v_add_u32_e32 v18, v18, v12
	s_waitcnt vmcnt(3)
	v_add_u32_e32 v18, v18, v13
	s_waitcnt vmcnt(2)
	v_add_u32_e32 v18, v18, v14
	s_waitcnt vmcnt(1)
	v_add_u32_e32 v18, v18, v15
	s_waitcnt vmcnt(0)
	v_add_u32_e32 v18, v18, v16
	v_cmp_eq_u32_e32 vcc, s2, v18
	s_cbranch_vccnz .LBB0_360
	s_and_b32 s4, s3, 0xff
	s_cmp_eq_u32 s4, 0
	s_mov_b64 s[38:39], -1
	s_sleep 8
	s_cbranch_scc0 .LBB0_365
	global_load_dword v18, v211, s[84:85] sc1
	s_waitcnt vmcnt(0)
	v_cmp_eq_u32_e32 vcc, 0, v18
	s_cbranch_vccnz .LBB0_367
	s_mov_b64 s[38:39], 0

.LBB0_493:
	global_load_dword v17, v211, s[96:97] offset:1024 sc1
	global_load_dword v2, v211, s[96:97] offset:1280 sc1
	global_load_dword v3, v211, s[96:97] offset:1536 sc1
	global_load_dword v4, v211, s[96:97] offset:1792 sc1
	global_load_dword v5, v211, s[96:97] offset:2048 sc1
	global_load_dword v6, v211, s[96:97] offset:2304 sc1
	global_load_dword v7, v211, s[96:97] offset:2560 sc1
	global_load_dword v8, v211, s[96:97] offset:2816 sc1
	global_load_dword v9, v211, s[96:97] offset:3072 sc1
	global_load_dword v10, v211, s[96:97] offset:3328 sc1
	global_load_dword v11, v211, s[96:97] offset:3584 sc1
	global_load_dword v12, v211, s[96:97] offset:3840 sc1
	global_load_dword v13, v211, s[66:67] sc1
	global_load_dword v14, v211, s[28:29] sc1
	global_load_dword v15, v211, s[46:47] sc1
	global_load_dword v16, v211, s[64:65] sc1
	s_mov_b64 s[10:11], -1
	s_mov_b64 s[24:25], -1
	s_waitcnt vmcnt(14)
	v_add_u32_e32 v18, v2, v17
	s_waitcnt vmcnt(13)
	v_add_u32_e32 v18, v18, v3
	s_waitcnt vmcnt(12)
	v_add_u32_e32 v18, v18, v4
	s_waitcnt vmcnt(11)
	v_add_u32_e32 v18, v18, v5
	s_waitcnt vmcnt(10)
	v_add_u32_e32 v18, v18, v6
	s_waitcnt vmcnt(9)
	v_add_u32_e32 v18, v18, v7
	s_waitcnt vmcnt(8)
	v_add_u32_e32 v18, v18, v8
	s_waitcnt vmcnt(7)
	v_add_u32_e32 v18, v18, v9
	s_waitcnt vmcnt(6)
	v_add_u32_e32 v18, v18, v10
	s_waitcnt vmcnt(5)
	v_add_u32_e32 v18, v18, v11
	s_waitcnt vmcnt(4)
	v_add_u32_e32 v18, v18, v12
	s_waitcnt vmcnt(3)
	v_add_u32_e32 v18, v18, v13
	s_waitcnt vmcnt(2)
	v_add_u32_e32 v18, v18, v14
	s_waitcnt vmcnt(1)
	v_add_u32_e32 v18, v18, v15
	s_waitcnt vmcnt(0)
	v_add_u32_e32 v18, v18, v16
	v_cmp_eq_u32_e32 vcc, s2, v18
	s_cbranch_vccnz .LBB0_492
	s_and_b32 s4, s3, 0xff
	s_cmp_eq_u32 s4, 0
	s_mov_b64 s[34:35], -1
	s_sleep 8
	s_cbranch_scc0 .LBB0_497
	v_readlane_b32 s4, v255, 52
	v_readlane_b32 s5, v255, 53
	s_nop 4
	global_load_dword v18, v211, s[4:5] sc1
	s_waitcnt vmcnt(0)
	v_cmp_eq_u32_e32 vcc, 0, v18
	s_cbranch_vccnz .LBB0_499
	s_mov_b64 s[34:35], 0

.LBB0_509:
	s_and_b32 s3, s2, 0xff
	s_mov_b64 s[40:41], -1
	s_cmp_lg_u32 s3, 0
	s_mov_b64 s[50:51], -1
	s_sleep 8
	s_cbranch_scc1 .LBB0_512
	v_readlane_b32 s4, v255, 52
	v_readlane_b32 s5, v255, 53
	s_nop 4
	global_load_dword v2, v211, s[4:5] sc1
	s_waitcnt vmcnt(0)
	v_cmp_eq_u32_e32 vcc, 0, v2
	s_cbranch_vccnz .LBB0_514
	s_mov_b64 s[50:51], 0
	s_mov_b64 s[42:43], -1

.LBB0_904:
	global_load_dword v17, v211, s[96:97] offset:1024 sc1
	global_load_dword v2, v211, s[96:97] offset:1280 sc1
	global_load_dword v3, v211, s[96:97] offset:1536 sc1
	global_load_dword v4, v211, s[96:97] offset:1792 sc1
	global_load_dword v5, v211, s[96:97] offset:2048 sc1
	global_load_dword v6, v211, s[96:97] offset:2304 sc1
	global_load_dword v7, v211, s[96:97] offset:2560 sc1
	global_load_dword v8, v211, s[96:97] offset:2816 sc1
	global_load_dword v9, v211, s[96:97] offset:3072 sc1
	global_load_dword v10, v211, s[96:97] offset:3328 sc1
	global_load_dword v11, v211, s[96:97] offset:3584 sc1
	global_load_dword v12, v211, s[96:97] offset:3840 sc1
	global_load_dword v13, v211, s[66:67] sc1
	global_load_dword v14, v211, s[28:29] sc1
	global_load_dword v15, v211, s[46:47] sc1
	global_load_dword v16, v211, s[64:65] sc1
	s_mov_b64 s[10:11], -1
	s_mov_b64 s[24:25], -1
	s_waitcnt vmcnt(14)
	v_add_u32_e32 v18, v2, v17
	s_waitcnt vmcnt(13)
	v_add_u32_e32 v18, v18, v3
	s_waitcnt vmcnt(12)
	v_add_u32_e32 v18, v18, v4
	s_waitcnt vmcnt(11)
	v_add_u32_e32 v18, v18, v5
	s_waitcnt vmcnt(10)
	v_add_u32_e32 v18, v18, v6
	s_waitcnt vmcnt(9)
	v_add_u32_e32 v18, v18, v7
	s_waitcnt vmcnt(8)
	v_add_u32_e32 v18, v18, v8
	s_waitcnt vmcnt(7)
	v_add_u32_e32 v18, v18, v9
	s_waitcnt vmcnt(6)
	v_add_u32_e32 v18, v18, v10
	s_waitcnt vmcnt(5)
	v_add_u32_e32 v18, v18, v11
	s_waitcnt vmcnt(4)
	v_add_u32_e32 v18, v18, v12
	s_waitcnt vmcnt(3)
	v_add_u32_e32 v18, v18, v13
	s_waitcnt vmcnt(2)
	v_add_u32_e32 v18, v18, v14
	s_waitcnt vmcnt(1)
	v_add_u32_e32 v18, v18, v15
	s_waitcnt vmcnt(0)
	v_add_u32_e32 v18, v18, v16
	v_cmp_eq_u32_e32 vcc, s2, v18
	s_cbranch_vccnz .LBB0_903
	s_and_b32 s4, s3, 0xff
	s_cmp_eq_u32 s4, 0
	s_mov_b64 s[30:31], -1
	s_sleep 8
	s_cbranch_scc0 .LBB0_908
	global_load_dword v18, v211, s[84:85] sc1
	s_waitcnt vmcnt(0)
	v_cmp_eq_u32_e32 vcc, 0, v18
	s_cbranch_vccnz .LBB0_910
	s_mov_b64 s[30:31], 0

.LBB0_920:
	s_and_b32 s3, s2, 0xff
	s_mov_b64 s[38:39], -1
	s_cmp_lg_u32 s3, 0
	s_mov_b64 s[42:43], -1
	s_sleep 8
	s_cbranch_scc1 .LBB0_923
	global_load_dword v2, v211, s[84:85] sc1
	s_waitcnt vmcnt(0)
	v_cmp_eq_u32_e32 vcc, 0, v2
	s_cbranch_vccnz .LBB0_925
	s_mov_b64 s[42:43], 0
	s_mov_b64 s[40:41], -1
